# MoE: LDS slots of unstaged padding rows zeroed once per unit so their MFMAs run on zeros (results of those rows are never used)
# baseline (speedup 1.0000x reference)
; #define MG_STAGE_A(b, rows, k0) do { _Pragma("unroll") for (int h_ = 0; h_ < 2; ++h_) _Pragma("unroll") for (int i_ = 0; i_ < 2; ++i_) if (rows[h_][i_] != 0xffffffffu) \
;         __builtin_amdgcn_global_load_lds((const unsigned*)((const char*)Abase + rows[h_][i_] + (k0) * 2), (PG8_LAS unsigned*)(lds + MG_SA(b, h_) + ldsw + i_ * 8192), 16, 0, 0); } while (0)
; template <class Epi, bool G1> ...
;     ...
;             else if (has_next) { MG_ROWS(nxt, rowC); MG_STAGE_A(buf ^ 1, rowC, 0); }
.LBB0_1073:
	v_mov_b32_e32 v199, v197
	v_mov_b32_e32 v193, v197
	v_mov_b32_e32 v195, v197
	s_xor_b64 s[38:39], s[40:41], -1
	v_lshl_add_u64 v[206:207], v[196:197], 0, s[30:31]
	v_lshl_add_u64 v[208:209], v[198:199], 0, s[30:31]
	v_lshl_add_u64 v[210:211], v[192:193], 0, s[30:31]
	v_lshl_add_u64 v[212:213], v[194:195], 0, s[30:31]
	v_cmp_ne_u32_e64 s[14:15], -1, v194
	v_cmp_ne_u32_e64 s[12:13], -1, v192
	v_cmp_ne_u32_e64 s[8:9], -1, v198
	v_cmp_ne_u32_e64 s[6:7], -1, v196
	v_mbcnt_lo_u32_b32 v226, -1, 0
	v_mbcnt_hi_u32_b32 v226, -1, v226
	v_lshl_add_u32 v226, v226, 4, s51
	v_mov_b32_e32 v228, 0
	v_mov_b32_e32 v229, 0
	v_mov_b32_e32 v230, 0
	v_mov_b32_e32 v231, 0
	s_andn2_b64 exec, exec, s[14:15]
	ds_write_b128 v226, v[228:231]
	ds_write_b128 v226, v[228:231] offset:32768
	s_mov_b64 exec, -1
	s_andn2_b64 exec, exec, s[12:13]
	ds_write_b128 v226, v[228:231] offset:8192
	ds_write_b128 v226, v[228:231] offset:40960
	s_mov_b64 exec, -1
	s_andn2_b64 exec, exec, s[8:9]
	ds_write_b128 v226, v[228:231] offset:16384
	ds_write_b128 v226, v[228:231] offset:49152
	s_mov_b64 exec, -1
	s_andn2_b64 exec, exec, s[6:7]
	ds_write_b128 v226, v[228:231] offset:24576
	ds_write_b128 v226, v[228:231] offset:57344
	s_mov_b64 exec, -1
	s_mov_b64 s[42:43], 0
	s_mov_b64 s[44:45], s[2:3]
	s_branch .LBB0_1075

; #define MG_STAGE_A(b, rows, k0) do { _Pragma("unroll") for (int h_ = 0; h_ < 2; ++h_) _Pragma("unroll") for (int i_ = 0; i_ < 2; ++i_) if (rows[h_][i_] != 0xffffffffu) \
;         __builtin_amdgcn_global_load_lds((const unsigned*)((const char*)Abase + rows[h_][i_] + (k0) * 2), (PG8_LAS unsigned*)(lds + MG_SA(b, h_) + ldsw + i_ * 8192), 16, 0, 0); } while (0)
; template <class Epi, bool G1> ...
;     ...
;             else if (has_next) { MG_ROWS(nxt, rowC); MG_STAGE_A(buf ^ 1, rowC, 0); }
.LBB0_1262:
	v_mov_b32_e32 v203, v1
	v_mov_b32_e32 v201, v1
	v_mov_b32_e32 v199, v1
	s_xor_b64 s[16:17], s[46:47], -1
	v_lshl_add_u64 v[2:3], v[0:1], 0, s[40:41]
	v_lshl_add_u64 v[208:209], v[202:203], 0, s[40:41]
	v_lshl_add_u64 v[210:211], v[200:201], 0, s[40:41]
	v_lshl_add_u64 v[212:213], v[198:199], 0, s[40:41]
	v_cmp_ne_u32_e64 s[14:15], -1, v198
	v_cmp_ne_u32_e64 s[12:13], -1, v200
	v_cmp_ne_u32_e64 s[8:9], -1, v202
	v_cmp_ne_u32_e64 s[6:7], -1, v0
	v_mbcnt_lo_u32_b32 v226, -1, 0
	v_mbcnt_hi_u32_b32 v226, -1, v226
	v_lshl_add_u32 v226, v226, 4, s57
	v_mov_b32_e32 v228, 0
	v_mov_b32_e32 v229, 0
	v_mov_b32_e32 v230, 0
	v_mov_b32_e32 v231, 0
	s_andn2_b64 exec, exec, s[14:15]
	ds_write_b128 v226, v[228:231]
	ds_write_b128 v226, v[228:231] offset:32768
	s_mov_b64 exec, -1
	s_andn2_b64 exec, exec, s[12:13]
	ds_write_b128 v226, v[228:231] offset:8192
	ds_write_b128 v226, v[228:231] offset:40960
	s_mov_b64 exec, -1
	s_andn2_b64 exec, exec, s[8:9]
	ds_write_b128 v226, v[228:231] offset:16384
	ds_write_b128 v226, v[228:231] offset:49152
	s_mov_b64 exec, -1
	s_andn2_b64 exec, exec, s[6:7]
	ds_write_b128 v226, v[228:231] offset:24576
	ds_write_b128 v226, v[228:231] offset:57344
	s_mov_b64 exec, -1
	s_mov_b64 s[48:49], 0
	s_mov_b64 s[50:51], s[18:19]
	s_branch .LBB0_1264
